# second barrier replaced by per-wave flags, row blocks in the original order (wave waits only for block i's delta)
# speedup vs baseline: 1.0008x; 1.0008x over previous
.LBB0_3:
	s_mov_b32 s14, s46
	s_and_b32 s14, s14, 7
	s_lshl_b32 s13, s14, 25
	s_lshl_b32 s15, s14, 10
	v_add_u32_e32 v9, s15, v203
	s_lshl_b32 s15, s14, 2
	s_add_i32 s15, s15, 0x26800
	v_mov_b32_e32 v7, s15
